# adds hand-scheduled scan-B chunk loop: all LDS fragment reads up front, interleaved MFMA chains, state kept in place, progress published two groups behind the write-through stores
# speedup vs baseline: 1.0036x; 1.0036x over previous
; DI void phase_scan_b(Frame& F, int l) {
;     ...
;         for (int c = 0; c < 128; ++c) {
;             if (w >= 4) asm volatile("s_waitcnt vmcnt(28)" ::: "memory");
;             __builtin_amdgcn_s_barrier();
.LBB0_1258:
	s_add_i32 s13, s13, 1
	v_add_u32_e32 v68, 0x2000, v68
	s_cmpk_eq_i32 s13, 0x88
	s_cbranch_scc1 .LBB0_1270

; DI void phase_scan_b(Frame& F, int l) {
;     ...
;         for (int c = 0; c < 128; ++c) {
;             if (w >= 4) asm volatile("s_waitcnt vmcnt(28)" ::: "memory");
;             __builtin_amdgcn_s_barrier();
;             asm volatile("" ::: "memory");
;             if (w >= 4) {
;                 if (c >= 1) { const int cn = c - 1 + SB_D; scanb_issue(F.lds, r1, r2, cn < 128 ? cn : c, w - 4, lane); }
;             } else {
;                 const LAS unsigned char* slot = F.lds + (c % SB_D) * SB_SLOT;
;                 bf16x8 pm[4][2]; f32x4 q[4];
; #pragma unroll
;                 for (int mt = 0; mt < 4; ++mt) { const int row = 16 * mt + r16;
; #pragma unroll
;                     for (int s2 = 0; s2 < 2; ++s2) pm[mt][s2] = *(const LAS bf16x8*)(slot + row * 128 + (((4 * s2 + g) ^ (row & 7)) << 4));
;                     { const u32x2 qw = *(const LAS u32x2*)(slot + 8192 + v * 128 + (((2 * mt + (g >> 1)) ^ (v & 7)) << 4) + (g & 1) * 8); q[mt] = (f32x4){bflo(qw.x), bfhi(qw.x), bflo(qw.y), bfhi(qw.y)}; } }
;                 bf16x8 hi[2], lo[2];
; #pragma unroll
;                 for (int s2 = 0; s2 < 2; ++s2) { u32x4 hw, lw;
; #pragma unroll
;                     for (int qq = 0; qq < 2; ++qq) { const f32x4 x = sT[2 * s2 + qq]; const unsigned h0 = pk2(x[0], x[1]), h1 = pk2(x[2], x[3]);
;                         const unsigned l0 = pk2(x[0] - bflo(h0), x[1] - bfhi(h0)), l1 = pk2(x[2] - bflo(h1), x[3] - bfhi(h1));
;                         if (qq == 0) { hw.x = h0; hw.y = h1; lw.x = l0; lw.y = l1; } else { hw.z = h0; hw.w = h1; lw.z = l0; lw.w = l1; } }
;                     hi[s2] = __builtin_bit_cast(bf16x8, hw); lo[s2] = __builtin_bit_cast(bf16x8, lw);
;                     __builtin_amdgcn_raw_buffer_store_b128(hw, srs, (int)(((unsigned)c * 4096u + (unsigned)v * 64u + 32u * s2 + 8u * g) * 2u), 0, 16); }
; #pragma unroll
;                 for (int mt = 0; mt < 4; ++mt) { f32x4 n = q[mt];
; #pragma unroll
;                     for (int s2 = 0; s2 < 2; ++s2) { n = mfma16(pm[mt][s2], hi[s2], n); n = mfma16(pm[mt][s2], lo[s2], n); }
;                     sT[mt] = n; }
;                 asm volatile("s_waitcnt lgkmcnt(0)" ::: "memory");
;                 if ((c & 3) == 3 && c >= 7) { asm volatile("s_waitcnt vmcnt(8)" ::: "memory");
;                     if (lane == 0) __hip_atomic_fetch_add(flg, 1u, __ATOMIC_RELAXED, __HIP_MEMORY_SCOPE_AGENT); }
.Lsb_bar:
	s_barrier
	s_add_i32 s41, s13, -8
	s_and_b64 vcc, exec, s[8:9]
	s_cbranch_vccz .Lsb_loader
	s_mul_i32 s16, s41, 57
	s_bfe_u32 s16, s16, 0x70009
	s_mul_i32 s16, s16, 9
	s_sub_i32 s16, s41, s16
	s_and_b32 s16, s16, 0xff
	s_lshl_b32 s16, s16, 14
	s_add_i32 s16, s83, s16
	v_add3_u32 v69, s16, v53, v54
	v_add_u32_e32 v178, s16, v52
	v_add_u32_e32 v222, v69, v58
	v_add_u32_e32 v223, v69, v59
	v_add_u32_e32 v179, v69, v60
	v_add_u32_e32 v69, v69, v61
	v_add_u32_e32 v82, v178, v56
	v_add_u32_e32 v178, v178, v57
	ds_read_b64 v[198:199], v222 offset:8192
	ds_read_b64 v[200:201], v223 offset:8192
	ds_read_b64 v[202:203], v179 offset:8192
	ds_read_b64 v[204:205], v69 offset:8192
	ds_read_b128 v[36:39], v82
	ds_read_b128 v[40:43], v82 offset:2048
	ds_read_b128 v[70:73], v82 offset:4096
	ds_read_b128 v[74:77], v82 offset:6144
	ds_read_b128 v[180:183], v178
	ds_read_b128 v[184:187], v178 offset:2048
	ds_read_b128 v[188:191], v178 offset:4096
	ds_read_b128 v[192:195], v178 offset:6144
	v_readlane_b32 s16, v252, 11
	v_readlane_b32 s17, v252, 12
	v_readlane_b32 s18, v252, 13
	v_readlane_b32 s19, v252, 14
	v_cvt_pk_bf16_f32 v20, v0, v1
	v_cvt_pk_bf16_f32 v21, v2, v3
	v_cvt_pk_bf16_f32 v22, v4, v5
	v_cvt_pk_bf16_f32 v23, v6, v7
	v_cvt_pk_bf16_f32 v24, v8, v9
	v_cvt_pk_bf16_f32 v25, v10, v11
	v_cvt_pk_bf16_f32 v26, v12, v13
	v_cvt_pk_bf16_f32 v27, v14, v15
	v_subrev_u32_e32 v197, 64, v68
	buffer_store_dwordx4 v[20:23], v197, s[16:19], 0 offen sc1
	buffer_store_dwordx4 v[24:27], v68, s[16:19], 0 offen sc1
	v_lshlrev_b32_e32 v16, 16, v20
	v_and_b32_e32 v17, 0xffff0000, v20
	v_lshlrev_b32_e32 v18, 16, v21
	v_and_b32_e32 v19, 0xffff0000, v21
	v_lshlrev_b32_e32 v78, 16, v22
	v_and_b32_e32 v79, 0xffff0000, v22
	v_lshlrev_b32_e32 v80, 16, v23
	v_and_b32_e32 v81, 0xffff0000, v23
	v_pk_add_f32 v[16:17], v[0:1], v[16:17] neg_lo:[0,1] neg_hi:[0,1]
	v_pk_add_f32 v[18:19], v[2:3], v[18:19] neg_lo:[0,1] neg_hi:[0,1]
	v_pk_add_f32 v[78:79], v[4:5], v[78:79] neg_lo:[0,1] neg_hi:[0,1]
	v_pk_add_f32 v[80:81], v[6:7], v[80:81] neg_lo:[0,1] neg_hi:[0,1]
	v_cvt_pk_bf16_f32 v32, v16, v17
	v_cvt_pk_bf16_f32 v33, v18, v19
	v_cvt_pk_bf16_f32 v34, v78, v79
	v_cvt_pk_bf16_f32 v35, v80, v81
	v_lshlrev_b32_e32 v16, 16, v24
	v_and_b32_e32 v17, 0xffff0000, v24
	v_lshlrev_b32_e32 v18, 16, v25
	v_and_b32_e32 v19, 0xffff0000, v25
	v_lshlrev_b32_e32 v78, 16, v26
	v_and_b32_e32 v79, 0xffff0000, v26
	v_lshlrev_b32_e32 v80, 16, v27
	v_and_b32_e32 v81, 0xffff0000, v27
	v_pk_add_f32 v[16:17], v[8:9], v[16:17] neg_lo:[0,1] neg_hi:[0,1]
	v_pk_add_f32 v[18:19], v[10:11], v[18:19] neg_lo:[0,1] neg_hi:[0,1]
	v_pk_add_f32 v[78:79], v[12:13], v[78:79] neg_lo:[0,1] neg_hi:[0,1]
	v_pk_add_f32 v[80:81], v[14:15], v[80:81] neg_lo:[0,1] neg_hi:[0,1]
	v_cvt_pk_bf16_f32 v28, v16, v17
	v_cvt_pk_bf16_f32 v29, v18, v19
	v_cvt_pk_bf16_f32 v30, v78, v79
	v_cvt_pk_bf16_f32 v31, v80, v81
	s_waitcnt lgkmcnt(8)
	v_lshlrev_b32_e32 v206, 16, v198
	v_and_b32_e32 v207, 0xffff0000, v198
	v_lshlrev_b32_e32 v208, 16, v199
	v_and_b32_e32 v209, 0xffff0000, v199
	v_lshlrev_b32_e32 v210, 16, v200
	v_and_b32_e32 v211, 0xffff0000, v200
	v_lshlrev_b32_e32 v212, 16, v201
	v_and_b32_e32 v213, 0xffff0000, v201
	v_lshlrev_b32_e32 v214, 16, v202
	v_and_b32_e32 v215, 0xffff0000, v202
	v_lshlrev_b32_e32 v216, 16, v203
	v_and_b32_e32 v217, 0xffff0000, v203
	v_lshlrev_b32_e32 v218, 16, v204
	v_and_b32_e32 v219, 0xffff0000, v204
	v_lshlrev_b32_e32 v220, 16, v205
	v_and_b32_e32 v221, 0xffff0000, v205
	s_waitcnt lgkmcnt(4)
	s_nop 0
	v_mfma_f32_16x16x32_bf16 v[0:3], v[36:39], v[20:23], v[206:209]
	v_mfma_f32_16x16x32_bf16 v[4:7], v[40:43], v[20:23], v[210:213]
	v_mfma_f32_16x16x32_bf16 v[8:11], v[70:73], v[20:23], v[214:217]
	v_mfma_f32_16x16x32_bf16 v[12:15], v[74:77], v[20:23], v[218:221]
	v_mfma_f32_16x16x32_bf16 v[0:3], v[36:39], v[32:35], v[0:3]
	v_mfma_f32_16x16x32_bf16 v[4:7], v[40:43], v[32:35], v[4:7]
	v_mfma_f32_16x16x32_bf16 v[8:11], v[70:73], v[32:35], v[8:11]
	v_mfma_f32_16x16x32_bf16 v[12:15], v[74:77], v[32:35], v[12:15]
	s_waitcnt lgkmcnt(0)
	v_mfma_f32_16x16x32_bf16 v[0:3], v[180:183], v[24:27], v[0:3]
	v_mfma_f32_16x16x32_bf16 v[4:7], v[184:187], v[24:27], v[4:7]
	v_mfma_f32_16x16x32_bf16 v[8:11], v[188:191], v[24:27], v[8:11]
	v_mfma_f32_16x16x32_bf16 v[12:15], v[192:195], v[24:27], v[12:15]
	v_mfma_f32_16x16x32_bf16 v[0:3], v[180:183], v[28:31], v[0:3]
	v_mfma_f32_16x16x32_bf16 v[4:7], v[184:187], v[28:31], v[4:7]
	v_mfma_f32_16x16x32_bf16 v[8:11], v[188:191], v[28:31], v[8:11]
	v_mfma_f32_16x16x32_bf16 v[12:15], v[192:195], v[28:31], v[12:15]
	s_and_b32 s16, s41, 3
	s_cmp_eq_u32 s16, 3
	s_cselect_b64 s[16:17], -1, 0
	s_cmp_gt_u32 s41, 10
	s_cselect_b64 s[18:19], -1, 0
	s_and_b64 s[16:17], s[16:17], s[18:19]
	s_andn2_b64 vcc, exec, s[16:17]
	s_cbranch_vccnz .LBB0_1258
	s_waitcnt vmcnt(16)
	s_and_saveexec_b64 s[16:17], s[0:1]
	s_cbranch_execz .Lsb_flag_done
	s_mov_b64 s[18:19], exec
	v_mbcnt_lo_u32_b32 v16, s18, 0
	v_mbcnt_hi_u32_b32 v16, s19, v16
	v_cmp_eq_u32_e32 vcc, 0, v16
	s_and_b64 s[42:43], exec, vcc
	s_mov_b64 exec, s[42:43]
	s_cbranch_execz .Lsb_flag_done
	s_bcnt1_i32_b64 s18, s[18:19]
	v_mov_b32_e32 v16, s18
	global_atomic_add v65, v16, s[14:15]
.Lsb_flag_done:
	s_or_b64 exec, exec, s[16:17]
	s_branch .LBB0_1258
.Lsb_loader:
	s_cmpk_lt_u32 s41, 0x78
	s_cselect_b32 s16, s13, s41
	s_mul_i32 s17, s16, 57
	s_bfe_u32 s17, s17, 0x70009
	s_mul_i32 s17, s17, 9
	s_lshl_b32 s44, s16, 14
	s_sub_i32 s16, s16, s17
	s_and_b32 s16, s16, 0xff
	s_lshl_b32 s16, s16, 14
	s_add_i32 s16, s83, s16
	v_lshl_add_u64 v[16:17], v[48:49], 0, s[44:45]
	v_lshl_add_u64 v[18:19], v[16:17], 0, v[44:45]
	s_add_i32 m0, s16, s33
	v_lshl_add_u64 v[16:17], v[16:17], 0, v[46:47]
	global_load_lds_dwordx4 v[18:19], off
	s_add_i32 m0, s16, s34
	s_add_i32 s16, s16, s31
	global_load_lds_dwordx4 v[16:17], off
	v_lshl_add_u64 v[16:17], v[50:51], 0, s[44:45]
	v_lshl_add_u64 v[18:19], v[16:17], 0, v[44:45]
	s_mov_b32 m0, s16
	v_lshl_add_u64 v[16:17], v[16:17], 0, v[46:47]
	global_load_lds_dwordx4 v[18:19], off
	s_add_i32 m0, s16, 0x400
	s_nop 0
	global_load_lds_dwordx4 v[16:17], off
	s_branch .LBB0_1258
.LBB0_1270:
	s_waitcnt vmcnt(0)
	s_and_saveexec_b64 s[2:3], s[10:11]
	s_cbranch_execz .LBB0_1250
	s_mov_b64 s[16:17], exec
	v_mbcnt_lo_u32_b32 v0, s16, 0
	v_mbcnt_hi_u32_b32 v0, s17, v0
	v_cmp_eq_u32_e32 vcc, 0, v0
	s_and_b64 s[18:19], exec, vcc
	s_mov_b64 exec, s[18:19]
	s_cbranch_execz .LBB0_1250
	s_bcnt1_i32_b64 s13, s[16:17]
	s_lshl_b32 s13, s13, 1
	v_mov_b32_e32 v0, s13
	global_atomic_add v65, v0, s[14:15]
	s_branch .LBB0_1250
